# v31: attention-phase weight-conversion items shared over all four kv-group classes (72/50/12/12 per workgroup instead of 84/62/0/0); conv pads kept
# speedup vs baseline: 1.0049x; 1.0049x over previous
; #define LAS __attribute__((address_space(3)))
; __global__ void __launch_bounds__(NWAVES * 64, 2) mega_fwd(Args args) {
;     ...
;         if (F.G == 256) { const int pq = blockIdx.x, bg_ = (pq & 7) * 2 + ((pq >> 3) & 1), g_ = bg_ & 3, li = (bg_ >> 2) * 16 + (pq >> 4);
;             if (g_ < 2) { const int cnt = g_ == 0 ? TR_AT0 : TR_AT1, first = g_ == 0 ? li * TR_AT0 : 64 * TR_AT0 + li * TR_AT1;
;                 tr_run<2>(F, first + F.wave, first + cnt, NWAVES, (LAS float*)(F.lds + RING_OFF + F.wave * 16384)); }
.LBB0_1331:
	s_mov_b64 s[86:87], s[18:19]
	v_readlane_b32 s66, v248, 20
	s_cmpk_eq_i32 s89, 0x100
	v_readlane_b32 s92, v248, 14
	s_mov_b64 s[84:85], s[16:17]
	s_mov_b64 s[82:83], s[14:15]
	s_mov_b64 s[80:81], s[12:13]
	s_mov_b64 s[78:79], s[10:11]
	v_readlane_b32 s67, v248, 21
	s_waitcnt lgkmcnt(0)
	s_barrier
	s_cbranch_scc0 .LBB0_1489
	v_readlane_b32 s0, v249, 37
	s_and_b32 s4, s0, 48
	s_ashr_i32 s0, s92, 4
	s_add_i32 s4, s4, s0
	s_bfe_u32 s2, s92, 0x10003
	s_and_b32 s0, s92, 1
	s_lshl_b32 s0, s0, 1
	s_or_b32 s2, s2, s0
	s_mov_b32 s17, 0x48
	s_mov_b32 s16, 0
	s_cmp_eq_u32 s2, 1
	s_cselect_b32 s17, 50, s17
	s_cselect_b32 s16, 0x1200, s16
	s_cmp_eq_u32 s2, 2
	s_cselect_b32 s17, 12, s17
	s_cselect_b32 s16, 0x1e80, s16
	s_cmp_eq_u32 s2, 3
	s_cselect_b32 s17, 12, s17
	s_cselect_b32 s16, 0x2180, s16
	s_mul_i32 s0, s4, s17
	s_add_i32 s16, s16, s0
	v_readlane_b32 s0, v249, 36
	s_cmp_lt_u32 s0, s17
	s_cselect_b64 s[14:15], -1, 0
	s_and_b64 vcc, exec, s[14:15]
	s_cbranch_vccnz .LBB0_1339
	v_lshrrev_b32_e32 v130, 3, v180
	v_lshlrev_b32_e32 v1, 2, v0
	v_and_b32_e32 v132, 28, v1
	v_mov_b32_e32 v133, 0
	v_or_b32_e32 v134, 64, v130
	s_mov_b64 s[0:1], 0
	s_branch .LBB0_1340
